# MOE_BLK0 (start of the three MoE phases): expert block prefix sums by one LDS read per lane + DPP scan instead of 32 dependent exec-masked LDS reads
# speedup vs baseline: 1.0088x; 1.0088x over previous
.LBB0_3189:
	s_or_b64 exec, exec, s[0:1]
	s_add_i32 s26, s20, 0x201c0
	v_cmp_gt_i32_e32 vcc, 33, v129
	s_waitcnt vmcnt(0) lgkmcnt(0)
	s_barrier
	s_and_saveexec_b64 s[0:1], vcc
	s_cbranch_execz .LBB0_3255
	s_mov_b64 s[4:5], exec
	s_mov_b64 exec, -1
	v_min_u32_e32 v1, 31, v129
	v_lshl_add_u32 v1, v1, 2, s25
	ds_read_b32 v0, v1
	v_cmp_gt_u32_e32 vcc, 32, v129
	s_waitcnt lgkmcnt(0)
	v_add_u32_e32 v0, 0xff, v0
	v_ashrrev_i32_e32 v0, 8, v0
	v_cndmask_b32_e32 v0, 0, v0, vcc
	s_nop 1
	v_add_u32_dpp v2, v0, v0 row_shr:1 row_mask:0xf bank_mask:0xf bound_ctrl:1
	s_nop 1
	v_add_u32_dpp v2, v2, v2 row_shr:2 row_mask:0xf bank_mask:0xf bound_ctrl:1
	s_nop 1
	v_add_u32_dpp v2, v2, v2 row_shr:4 row_mask:0xf bank_mask:0xf bound_ctrl:1
	s_nop 1
	v_add_u32_dpp v2, v2, v2 row_shr:8 row_mask:0xf bank_mask:0xf bound_ctrl:1
	s_nop 1
	v_add_u32_dpp v2, v2, v2 row_bcast:15 row_mask:0xa bank_mask:0xf
	s_nop 1
	v_add_u32_dpp v2, v2, v2 row_bcast:31 row_mask:0xc bank_mask:0xf
	s_mov_b64 exec, s[4:5]
	v_sub_u32_e32 v0, v2, v0
	v_lshl_add_u32 v1, v129, 2, s26
	ds_write_b32 v1, v0
	s_add_i32 s7, s20, 0x202cc

.LBB0_3349:
	s_or_b64 exec, exec, s[0:1]
	v_cmp_gt_i32_e32 vcc, 33, v129
	s_waitcnt vmcnt(0) lgkmcnt(0)
	s_barrier
	s_and_saveexec_b64 s[0:1], vcc
	s_cbranch_execz .LBB0_3415
	s_mov_b64 s[2:3], exec
	s_mov_b64 exec, -1
	v_min_u32_e32 v1, 31, v129
	v_lshl_add_u32 v1, v1, 2, s5
	ds_read_b32 v0, v1
	v_cmp_gt_u32_e32 vcc, 32, v129
	s_waitcnt lgkmcnt(0)
	v_add_u32_e32 v0, 0xff, v0
	v_ashrrev_i32_e32 v0, 8, v0
	v_cndmask_b32_e32 v0, 0, v0, vcc
	s_nop 1
	v_add_u32_dpp v2, v0, v0 row_shr:1 row_mask:0xf bank_mask:0xf bound_ctrl:1
	s_nop 1
	v_add_u32_dpp v2, v2, v2 row_shr:2 row_mask:0xf bank_mask:0xf bound_ctrl:1
	s_nop 1
	v_add_u32_dpp v2, v2, v2 row_shr:4 row_mask:0xf bank_mask:0xf bound_ctrl:1
	s_nop 1
	v_add_u32_dpp v2, v2, v2 row_shr:8 row_mask:0xf bank_mask:0xf bound_ctrl:1
	s_nop 1
	v_add_u32_dpp v2, v2, v2 row_bcast:15 row_mask:0xa bank_mask:0xf
	s_nop 1
	v_add_u32_dpp v2, v2, v2 row_bcast:31 row_mask:0xc bank_mask:0xf
	s_mov_b64 exec, s[2:3]
	v_sub_u32_e32 v0, v2, v0
	v_lshl_add_u32 v1, v129, 2, s14
	v_add_u32_e32 v1, 0x201c0, v1
	ds_write_b32 v1, v0
	s_add_i32 s5, s14, 0x202cc

.LBB0_3494:
	s_or_b64 exec, exec, s[4:5]
	s_add_i32 s26, s8, 0x201c0
	v_cmp_gt_i32_e32 vcc, 33, v126
	s_waitcnt vmcnt(0) lgkmcnt(0)
	s_barrier
	s_and_saveexec_b64 s[4:5], vcc
	s_cbranch_execz .LBB0_3560
	s_mov_b64 s[6:7], exec
	s_mov_b64 exec, -1
	v_min_u32_e32 v1, 31, v126
	v_lshl_add_u32 v1, v1, 2, s11
	ds_read_b32 v0, v1
	v_cmp_gt_u32_e32 vcc, 32, v126
	s_waitcnt lgkmcnt(0)
	v_add_u32_e32 v0, 0xff, v0
	v_ashrrev_i32_e32 v0, 8, v0
	v_cndmask_b32_e32 v0, 0, v0, vcc
	s_nop 1
	v_add_u32_dpp v2, v0, v0 row_shr:1 row_mask:0xf bank_mask:0xf bound_ctrl:1
	s_nop 1
	v_add_u32_dpp v2, v2, v2 row_shr:2 row_mask:0xf bank_mask:0xf bound_ctrl:1
	s_nop 1
	v_add_u32_dpp v2, v2, v2 row_shr:4 row_mask:0xf bank_mask:0xf bound_ctrl:1
	s_nop 1
	v_add_u32_dpp v2, v2, v2 row_shr:8 row_mask:0xf bank_mask:0xf bound_ctrl:1
	s_nop 1
	v_add_u32_dpp v2, v2, v2 row_bcast:15 row_mask:0xa bank_mask:0xf
	s_nop 1
	v_add_u32_dpp v2, v2, v2 row_bcast:31 row_mask:0xc bank_mask:0xf
	s_mov_b64 exec, s[6:7]
	v_sub_u32_e32 v0, v2, v0
	v_lshl_add_u32 v1, v126, 2, s26
	ds_write_b32 v1, v0
	s_add_i32 s11, s8, 0x202cc
